# combo7 + phase 10 contiguous-span layout with two tokens of loads in flight
# speedup vs baseline: 1.0145x; 1.0012x over previous
.LBB0_1219:
	s_cmp_lt_i32 s48, 11
	s_cselect_b64 s[6:7], -1, 0
	s_and_b64 s[4:5], s[6:7], s[4:5]
	s_andn2_b64 vcc, exec, s[4:5]
	s_cbranch_vccnz .LBB0_1225
	s_load_dwordx4 s[4:7], s[0:1], 0xa8
	v_and_b32_e32 v1, 63, v0
	v_lshrrev_b32_e32 v5, 6, v0
	s_lshl_b32 s13, s2, 3
	v_readfirstlane_b32 s12, v5
	v_lshlrev_b32_e32 v2, 2, v1
	v_lshlrev_b32_e32 v3, 3, v1
	v_lshlrev_b32_e32 v4, 4, v1
	s_add_i32 s12, s12, s13
	v_lshl_add_u32 v5, v1, 11, s12
	v_lshlrev_b32_e32 v5, 3, v5
	v_cmp_gt_u32_e32 vcc, 8, v1
	s_waitcnt lgkmcnt(0)
	s_add_u32 s8, s6, 0x33c0a000
	s_addc_u32 s9, s7, 0
	s_add_u32 s10, s6, 0x33c2a000
	s_addc_u32 s11, s7, 0
	s_add_u32 s48, s6, 0x4744a000
	s_addc_u32 s49, s7, 0
	s_add_u32 s60, s6, 0x2b80a000
	s_addc_u32 s61, s7, 0
	s_lshl_b32 s14, s12, 12
	s_add_u32 s62, s60, s14
	s_addc_u32 s63, s61, 0
	s_lshl_b32 s14, s12, 13
	s_add_u32 s64, s4, s14
	s_addc_u32 s65, s5, 0
	s_and_saveexec_b64 s[14:15], vcc
	global_load_dwordx2 v[6:7], v5, s[8:9]
	global_load_dwordx2 v[8:9], v5, s[10:11]
	s_waitcnt vmcnt(1)
	v_ashrrev_i32_e32 v10, 16, v6
	v_ashrrev_i32_e32 v11, 16, v7
	v_lshlrev_b32_e32 v10, 2, v10
	v_lshlrev_b32_e32 v11, 2, v11
	v_add_u32_e32 v10, 0x24140, v10
	v_add_u32_e32 v11, 0x24140, v11
	ds_read_b32 v10, v10
	ds_read_b32 v11, v11
	v_and_b32_e32 v6, 0xffff, v6
	v_and_b32_e32 v7, 0xffff, v7
	s_waitcnt lgkmcnt(0)
	v_lshl_add_u32 v6, v10, 8, v6
	v_lshl_add_u32 v7, v11, 8, v7
	s_waitcnt vmcnt(0)
	s_mov_b64 exec, s[14:15]
	s_nop 1
	v_readlane_b32 s16, v6, 0
	v_readlane_b32 s24, v7, 0
	v_readlane_b32 s32, v8, 0
	v_readlane_b32 s40, v9, 0
	v_readlane_b32 s17, v6, 1
	v_readlane_b32 s25, v7, 1
	v_readlane_b32 s33, v8, 1
	v_readlane_b32 s41, v9, 1
	v_readlane_b32 s18, v6, 2
	v_readlane_b32 s26, v7, 2
	v_readlane_b32 s34, v8, 2
	v_readlane_b32 s42, v9, 2
	v_readlane_b32 s19, v6, 3
	v_readlane_b32 s27, v7, 3
	v_readlane_b32 s35, v8, 3
	v_readlane_b32 s43, v9, 3
	v_readlane_b32 s20, v6, 4
	v_readlane_b32 s28, v7, 4
	v_readlane_b32 s36, v8, 4
	v_readlane_b32 s44, v9, 4
	v_readlane_b32 s21, v6, 5
	v_readlane_b32 s29, v7, 5
	v_readlane_b32 s37, v8, 5
	v_readlane_b32 s45, v9, 5
	v_readlane_b32 s22, v6, 6
	v_readlane_b32 s30, v7, 6
	v_readlane_b32 s38, v8, 6
	v_readlane_b32 s46, v9, 6
	v_readlane_b32 s23, v6, 7
	v_readlane_b32 s31, v7, 7
	v_readlane_b32 s39, v8, 7
	v_readlane_b32 s47, v9, 7
	s_nop 3
	s_lshl_b32 s50, s16, 11
	s_add_u32 s50, s48, s50
	s_addc_u32 s51, s49, 0
	s_lshl_b32 s52, s24, 11
	s_add_u32 s52, s48, s52
	s_addc_u32 s53, s49, 0
	s_mov_b64 s[54:55], s[62:63]
	global_load_dword v64, v2, s[50:51]
	global_load_dword v65, v2, s[50:51] offset:256
	global_load_dword v66, v2, s[50:51] offset:512
	global_load_dword v67, v2, s[50:51] offset:768
	global_load_dword v68, v2, s[50:51] offset:1024
	global_load_dword v69, v2, s[50:51] offset:1280
	global_load_dword v70, v2, s[50:51] offset:1536
	global_load_dword v71, v2, s[50:51] offset:1792
	global_load_dword v72, v2, s[52:53]
	global_load_dword v73, v2, s[52:53] offset:256
	global_load_dword v74, v2, s[52:53] offset:512
	global_load_dword v75, v2, s[52:53] offset:768
	global_load_dword v76, v2, s[52:53] offset:1024
	global_load_dword v77, v2, s[52:53] offset:1280
	global_load_dword v78, v2, s[52:53] offset:1536
	global_load_dword v79, v2, s[52:53] offset:1792
	global_load_dwordx2 v[80:81], v3, s[54:55]
	global_load_dwordx2 v[82:83], v3, s[54:55] offset:512
	global_load_dwordx2 v[84:85], v3, s[54:55] offset:1024
	global_load_dwordx2 v[86:87], v3, s[54:55] offset:1536
	global_load_dwordx2 v[88:89], v3, s[54:55] offset:2048
	global_load_dwordx2 v[90:91], v3, s[54:55] offset:2560
	global_load_dwordx2 v[92:93], v3, s[54:55] offset:3072
	global_load_dwordx2 v[94:95], v3, s[54:55] offset:3584
	s_lshl_b32 s50, s17, 11
	s_add_u32 s50, s48, s50
	s_addc_u32 s51, s49, 0
	s_lshl_b32 s52, s25, 11
	s_add_u32 s52, s48, s52
	s_addc_u32 s53, s49, 0
	s_add_u32 s54, s62, 0x800000
	s_addc_u32 s55, s63, 0
	global_load_dword v96, v2, s[50:51]
	global_load_dword v97, v2, s[50:51] offset:256
	global_load_dword v98, v2, s[50:51] offset:512
	global_load_dword v99, v2, s[50:51] offset:768
	global_load_dword v100, v2, s[50:51] offset:1024
	global_load_dword v101, v2, s[50:51] offset:1280
	global_load_dword v102, v2, s[50:51] offset:1536
	global_load_dword v103, v2, s[50:51] offset:1792
	global_load_dword v104, v2, s[52:53]
	global_load_dword v105, v2, s[52:53] offset:256
	global_load_dword v106, v2, s[52:53] offset:512
	global_load_dword v107, v2, s[52:53] offset:768
	global_load_dword v108, v2, s[52:53] offset:1024
	global_load_dword v109, v2, s[52:53] offset:1280
	global_load_dword v110, v2, s[52:53] offset:1536
	global_load_dword v111, v2, s[52:53] offset:1792
	global_load_dwordx2 v[112:113], v3, s[54:55]
	global_load_dwordx2 v[114:115], v3, s[54:55] offset:512
	global_load_dwordx2 v[116:117], v3, s[54:55] offset:1024
	global_load_dwordx2 v[118:119], v3, s[54:55] offset:1536
	global_load_dwordx2 v[120:121], v3, s[54:55] offset:2048
	global_load_dwordx2 v[122:123], v3, s[54:55] offset:2560
	global_load_dwordx2 v[124:125], v3, s[54:55] offset:3072
	global_load_dwordx2 v[126:127], v3, s[54:55] offset:3584
	s_waitcnt vmcnt(24)
	s_lshl_b32 s50, s18, 11
	s_add_u32 s50, s48, s50
	s_addc_u32 s51, s49, 0
	s_lshl_b32 s52, s26, 11
	s_add_u32 s52, s48, s52
	s_addc_u32 s53, s49, 0
	s_add_u32 s54, s62, 0x1000000
	s_addc_u32 s55, s63, 0
	global_load_dword v128, v2, s[50:51]
	global_load_dword v129, v2, s[50:51] offset:256
	global_load_dword v130, v2, s[50:51] offset:512
	global_load_dword v131, v2, s[50:51] offset:768
	global_load_dword v132, v2, s[50:51] offset:1024
	global_load_dword v133, v2, s[50:51] offset:1280
	global_load_dword v134, v2, s[50:51] offset:1536
	global_load_dword v135, v2, s[50:51] offset:1792
	global_load_dword v136, v2, s[52:53]
	global_load_dword v137, v2, s[52:53] offset:256
	global_load_dword v138, v2, s[52:53] offset:512
	global_load_dword v139, v2, s[52:53] offset:768
	global_load_dword v140, v2, s[52:53] offset:1024
	global_load_dword v141, v2, s[52:53] offset:1280
	global_load_dword v142, v2, s[52:53] offset:1536
	global_load_dword v143, v2, s[52:53] offset:1792
	global_load_dwordx2 v[144:145], v3, s[54:55]
	global_load_dwordx2 v[146:147], v3, s[54:55] offset:512
	global_load_dwordx2 v[148:149], v3, s[54:55] offset:1024
	global_load_dwordx2 v[150:151], v3, s[54:55] offset:1536
	global_load_dwordx2 v[152:153], v3, s[54:55] offset:2048
	global_load_dwordx2 v[154:155], v3, s[54:55] offset:2560
	global_load_dwordx2 v[156:157], v3, s[54:55] offset:3072
	global_load_dwordx2 v[158:159], v3, s[54:55] offset:3584
	v_mov_b32_e32 v240, s32
	v_mov_b32_e32 v242, s40
	v_cvt_pk_f32_fp8_e32 v[224:225], v64
	v_cvt_pk_f32_fp8_sdwa v[226:227], v64 src0_sel:WORD_1
	v_cvt_pk_f32_fp8_e32 v[228:229], v72
	v_cvt_pk_f32_fp8_sdwa v[230:231], v72 src0_sel:WORD_1
	v_lshlrev_b32_e32 v192, 16, v80
	v_and_b32_e32 v193, 0xffff0000, v80
	v_lshlrev_b32_e32 v194, 16, v81
	v_and_b32_e32 v195, 0xffff0000, v81
	v_pk_fma_f32 v[192:193], v[224:225], v[240:241], v[192:193] op_sel_hi:[1,0,1]
	v_pk_fma_f32 v[194:195], v[226:227], v[240:241], v[194:195] op_sel_hi:[1,0,1]
	v_pk_fma_f32 v[192:193], v[228:229], v[242:243], v[192:193] op_sel_hi:[1,0,1]
	v_pk_fma_f32 v[194:195], v[230:231], v[242:243], v[194:195] op_sel_hi:[1,0,1]
	v_cvt_pk_f32_fp8_e32 v[232:233], v65
	v_cvt_pk_f32_fp8_sdwa v[234:235], v65 src0_sel:WORD_1
	v_cvt_pk_f32_fp8_e32 v[236:237], v73
	v_cvt_pk_f32_fp8_sdwa v[238:239], v73 src0_sel:WORD_1
	v_lshlrev_b32_e32 v196, 16, v82
	v_and_b32_e32 v197, 0xffff0000, v82
	v_lshlrev_b32_e32 v198, 16, v83
	v_and_b32_e32 v199, 0xffff0000, v83
	v_pk_fma_f32 v[196:197], v[232:233], v[240:241], v[196:197] op_sel_hi:[1,0,1]
	v_pk_fma_f32 v[198:199], v[234:235], v[240:241], v[198:199] op_sel_hi:[1,0,1]
	v_pk_fma_f32 v[196:197], v[236:237], v[242:243], v[196:197] op_sel_hi:[1,0,1]
	v_pk_fma_f32 v[198:199], v[238:239], v[242:243], v[198:199] op_sel_hi:[1,0,1]
	v_cvt_pk_f32_fp8_e32 v[224:225], v66
	v_cvt_pk_f32_fp8_sdwa v[226:227], v66 src0_sel:WORD_1
	v_cvt_pk_f32_fp8_e32 v[228:229], v74
	v_cvt_pk_f32_fp8_sdwa v[230:231], v74 src0_sel:WORD_1
	v_lshlrev_b32_e32 v200, 16, v84
	v_and_b32_e32 v201, 0xffff0000, v84
	v_lshlrev_b32_e32 v202, 16, v85
	v_and_b32_e32 v203, 0xffff0000, v85
	v_pk_fma_f32 v[200:201], v[224:225], v[240:241], v[200:201] op_sel_hi:[1,0,1]
	v_pk_fma_f32 v[202:203], v[226:227], v[240:241], v[202:203] op_sel_hi:[1,0,1]
	v_pk_fma_f32 v[200:201], v[228:229], v[242:243], v[200:201] op_sel_hi:[1,0,1]
	v_pk_fma_f32 v[202:203], v[230:231], v[242:243], v[202:203] op_sel_hi:[1,0,1]
	v_cvt_pk_f32_fp8_e32 v[232:233], v67
	v_cvt_pk_f32_fp8_sdwa v[234:235], v67 src0_sel:WORD_1
	v_cvt_pk_f32_fp8_e32 v[236:237], v75
	v_cvt_pk_f32_fp8_sdwa v[238:239], v75 src0_sel:WORD_1
	v_lshlrev_b32_e32 v204, 16, v86
	v_and_b32_e32 v205, 0xffff0000, v86
	v_lshlrev_b32_e32 v206, 16, v87
	v_and_b32_e32 v207, 0xffff0000, v87
	v_pk_fma_f32 v[204:205], v[232:233], v[240:241], v[204:205] op_sel_hi:[1,0,1]
	v_pk_fma_f32 v[206:207], v[234:235], v[240:241], v[206:207] op_sel_hi:[1,0,1]
	v_pk_fma_f32 v[204:205], v[236:237], v[242:243], v[204:205] op_sel_hi:[1,0,1]
	v_pk_fma_f32 v[206:207], v[238:239], v[242:243], v[206:207] op_sel_hi:[1,0,1]
	v_cvt_pk_f32_fp8_e32 v[224:225], v68
	v_cvt_pk_f32_fp8_sdwa v[226:227], v68 src0_sel:WORD_1
	v_cvt_pk_f32_fp8_e32 v[228:229], v76
	v_cvt_pk_f32_fp8_sdwa v[230:231], v76 src0_sel:WORD_1
	v_lshlrev_b32_e32 v208, 16, v88
	v_and_b32_e32 v209, 0xffff0000, v88
	v_lshlrev_b32_e32 v210, 16, v89
	v_and_b32_e32 v211, 0xffff0000, v89
	v_pk_fma_f32 v[208:209], v[224:225], v[240:241], v[208:209] op_sel_hi:[1,0,1]
	v_pk_fma_f32 v[210:211], v[226:227], v[240:241], v[210:211] op_sel_hi:[1,0,1]
	v_pk_fma_f32 v[208:209], v[228:229], v[242:243], v[208:209] op_sel_hi:[1,0,1]
	v_pk_fma_f32 v[210:211], v[230:231], v[242:243], v[210:211] op_sel_hi:[1,0,1]
	v_cvt_pk_f32_fp8_e32 v[232:233], v69
	v_cvt_pk_f32_fp8_sdwa v[234:235], v69 src0_sel:WORD_1
	v_cvt_pk_f32_fp8_e32 v[236:237], v77
	v_cvt_pk_f32_fp8_sdwa v[238:239], v77 src0_sel:WORD_1
	v_lshlrev_b32_e32 v212, 16, v90
	v_and_b32_e32 v213, 0xffff0000, v90
	v_lshlrev_b32_e32 v214, 16, v91
	v_and_b32_e32 v215, 0xffff0000, v91
	v_pk_fma_f32 v[212:213], v[232:233], v[240:241], v[212:213] op_sel_hi:[1,0,1]
	v_pk_fma_f32 v[214:215], v[234:235], v[240:241], v[214:215] op_sel_hi:[1,0,1]
	v_pk_fma_f32 v[212:213], v[236:237], v[242:243], v[212:213] op_sel_hi:[1,0,1]
	v_pk_fma_f32 v[214:215], v[238:239], v[242:243], v[214:215] op_sel_hi:[1,0,1]
	v_cvt_pk_f32_fp8_e32 v[224:225], v70
	v_cvt_pk_f32_fp8_sdwa v[226:227], v70 src0_sel:WORD_1
	v_cvt_pk_f32_fp8_e32 v[228:229], v78
	v_cvt_pk_f32_fp8_sdwa v[230:231], v78 src0_sel:WORD_1
	v_lshlrev_b32_e32 v216, 16, v92
	v_and_b32_e32 v217, 0xffff0000, v92
	v_lshlrev_b32_e32 v218, 16, v93
	v_and_b32_e32 v219, 0xffff0000, v93
	v_pk_fma_f32 v[216:217], v[224:225], v[240:241], v[216:217] op_sel_hi:[1,0,1]
	v_pk_fma_f32 v[218:219], v[226:227], v[240:241], v[218:219] op_sel_hi:[1,0,1]
	v_pk_fma_f32 v[216:217], v[228:229], v[242:243], v[216:217] op_sel_hi:[1,0,1]
	v_pk_fma_f32 v[218:219], v[230:231], v[242:243], v[218:219] op_sel_hi:[1,0,1]
	v_cvt_pk_f32_fp8_e32 v[232:233], v71
	v_cvt_pk_f32_fp8_sdwa v[234:235], v71 src0_sel:WORD_1
	v_cvt_pk_f32_fp8_e32 v[236:237], v79
	v_cvt_pk_f32_fp8_sdwa v[238:239], v79 src0_sel:WORD_1
	v_lshlrev_b32_e32 v220, 16, v94
	v_and_b32_e32 v221, 0xffff0000, v94
	v_lshlrev_b32_e32 v222, 16, v95
	v_and_b32_e32 v223, 0xffff0000, v95
	v_pk_fma_f32 v[220:221], v[232:233], v[240:241], v[220:221] op_sel_hi:[1,0,1]
	v_pk_fma_f32 v[222:223], v[234:235], v[240:241], v[222:223] op_sel_hi:[1,0,1]
	v_pk_fma_f32 v[220:221], v[236:237], v[242:243], v[220:221] op_sel_hi:[1,0,1]
	v_pk_fma_f32 v[222:223], v[238:239], v[242:243], v[222:223] op_sel_hi:[1,0,1]
	s_waitcnt vmcnt(55)
	s_mov_b64 s[56:57], s[64:65]
	s_add_u32 s58, s56, 0x1000
	s_addc_u32 s59, s57, 0
	global_store_dwordx4 v4, v[192:195], s[56:57]
	global_store_dwordx4 v4, v[196:199], s[56:57] offset:1024
	global_store_dwordx4 v4, v[200:203], s[56:57] offset:2048
	global_store_dwordx4 v4, v[204:207], s[56:57] offset:3072
	global_store_dwordx4 v4, v[208:211], s[58:59]
	global_store_dwordx4 v4, v[212:215], s[58:59] offset:1024
	global_store_dwordx4 v4, v[216:219], s[58:59] offset:2048
	global_store_dwordx4 v4, v[220:223], s[58:59] offset:3072
	s_waitcnt vmcnt(32)
	s_lshl_b32 s50, s19, 11
	s_add_u32 s50, s48, s50
	s_addc_u32 s51, s49, 0
	s_lshl_b32 s52, s27, 11
	s_add_u32 s52, s48, s52
	s_addc_u32 s53, s49, 0
	s_add_u32 s54, s62, 0x1800000
	s_addc_u32 s55, s63, 0
	global_load_dword v64, v2, s[50:51]
	global_load_dword v65, v2, s[50:51] offset:256
	global_load_dword v66, v2, s[50:51] offset:512
	global_load_dword v67, v2, s[50:51] offset:768
	global_load_dword v68, v2, s[50:51] offset:1024
	global_load_dword v69, v2, s[50:51] offset:1280
	global_load_dword v70, v2, s[50:51] offset:1536
	global_load_dword v71, v2, s[50:51] offset:1792
	global_load_dword v72, v2, s[52:53]
	global_load_dword v73, v2, s[52:53] offset:256
	global_load_dword v74, v2, s[52:53] offset:512
	global_load_dword v75, v2, s[52:53] offset:768
	global_load_dword v76, v2, s[52:53] offset:1024
	global_load_dword v77, v2, s[52:53] offset:1280
	global_load_dword v78, v2, s[52:53] offset:1536
	global_load_dword v79, v2, s[52:53] offset:1792
	global_load_dwordx2 v[80:81], v3, s[54:55]
	global_load_dwordx2 v[82:83], v3, s[54:55] offset:512
	global_load_dwordx2 v[84:85], v3, s[54:55] offset:1024
	global_load_dwordx2 v[86:87], v3, s[54:55] offset:1536
	global_load_dwordx2 v[88:89], v3, s[54:55] offset:2048
	global_load_dwordx2 v[90:91], v3, s[54:55] offset:2560
	global_load_dwordx2 v[92:93], v3, s[54:55] offset:3072
	global_load_dwordx2 v[94:95], v3, s[54:55] offset:3584
	v_mov_b32_e32 v240, s33
	v_mov_b32_e32 v242, s41
	v_cvt_pk_f32_fp8_e32 v[224:225], v96
	v_cvt_pk_f32_fp8_sdwa v[226:227], v96 src0_sel:WORD_1
	v_cvt_pk_f32_fp8_e32 v[228:229], v104
	v_cvt_pk_f32_fp8_sdwa v[230:231], v104 src0_sel:WORD_1
	v_lshlrev_b32_e32 v192, 16, v112
	v_and_b32_e32 v193, 0xffff0000, v112
	v_lshlrev_b32_e32 v194, 16, v113
	v_and_b32_e32 v195, 0xffff0000, v113
	v_pk_fma_f32 v[192:193], v[224:225], v[240:241], v[192:193] op_sel_hi:[1,0,1]
	v_pk_fma_f32 v[194:195], v[226:227], v[240:241], v[194:195] op_sel_hi:[1,0,1]
	v_pk_fma_f32 v[192:193], v[228:229], v[242:243], v[192:193] op_sel_hi:[1,0,1]
	v_pk_fma_f32 v[194:195], v[230:231], v[242:243], v[194:195] op_sel_hi:[1,0,1]
	v_cvt_pk_f32_fp8_e32 v[232:233], v97
	v_cvt_pk_f32_fp8_sdwa v[234:235], v97 src0_sel:WORD_1
	v_cvt_pk_f32_fp8_e32 v[236:237], v105
	v_cvt_pk_f32_fp8_sdwa v[238:239], v105 src0_sel:WORD_1
	v_lshlrev_b32_e32 v196, 16, v114
	v_and_b32_e32 v197, 0xffff0000, v114
	v_lshlrev_b32_e32 v198, 16, v115
	v_and_b32_e32 v199, 0xffff0000, v115
	v_pk_fma_f32 v[196:197], v[232:233], v[240:241], v[196:197] op_sel_hi:[1,0,1]
	v_pk_fma_f32 v[198:199], v[234:235], v[240:241], v[198:199] op_sel_hi:[1,0,1]
	v_pk_fma_f32 v[196:197], v[236:237], v[242:243], v[196:197] op_sel_hi:[1,0,1]
	v_pk_fma_f32 v[198:199], v[238:239], v[242:243], v[198:199] op_sel_hi:[1,0,1]
	v_cvt_pk_f32_fp8_e32 v[224:225], v98
	v_cvt_pk_f32_fp8_sdwa v[226:227], v98 src0_sel:WORD_1
	v_cvt_pk_f32_fp8_e32 v[228:229], v106
	v_cvt_pk_f32_fp8_sdwa v[230:231], v106 src0_sel:WORD_1
	v_lshlrev_b32_e32 v200, 16, v116
	v_and_b32_e32 v201, 0xffff0000, v116
	v_lshlrev_b32_e32 v202, 16, v117
	v_and_b32_e32 v203, 0xffff0000, v117
	v_pk_fma_f32 v[200:201], v[224:225], v[240:241], v[200:201] op_sel_hi:[1,0,1]
	v_pk_fma_f32 v[202:203], v[226:227], v[240:241], v[202:203] op_sel_hi:[1,0,1]
	v_pk_fma_f32 v[200:201], v[228:229], v[242:243], v[200:201] op_sel_hi:[1,0,1]
	v_pk_fma_f32 v[202:203], v[230:231], v[242:243], v[202:203] op_sel_hi:[1,0,1]
	v_cvt_pk_f32_fp8_e32 v[232:233], v99
	v_cvt_pk_f32_fp8_sdwa v[234:235], v99 src0_sel:WORD_1
	v_cvt_pk_f32_fp8_e32 v[236:237], v107
	v_cvt_pk_f32_fp8_sdwa v[238:239], v107 src0_sel:WORD_1
	v_lshlrev_b32_e32 v204, 16, v118
	v_and_b32_e32 v205, 0xffff0000, v118
	v_lshlrev_b32_e32 v206, 16, v119
	v_and_b32_e32 v207, 0xffff0000, v119
	v_pk_fma_f32 v[204:205], v[232:233], v[240:241], v[204:205] op_sel_hi:[1,0,1]
	v_pk_fma_f32 v[206:207], v[234:235], v[240:241], v[206:207] op_sel_hi:[1,0,1]
	v_pk_fma_f32 v[204:205], v[236:237], v[242:243], v[204:205] op_sel_hi:[1,0,1]
	v_pk_fma_f32 v[206:207], v[238:239], v[242:243], v[206:207] op_sel_hi:[1,0,1]
	v_cvt_pk_f32_fp8_e32 v[224:225], v100
	v_cvt_pk_f32_fp8_sdwa v[226:227], v100 src0_sel:WORD_1
	v_cvt_pk_f32_fp8_e32 v[228:229], v108
	v_cvt_pk_f32_fp8_sdwa v[230:231], v108 src0_sel:WORD_1
	v_lshlrev_b32_e32 v208, 16, v120
	v_and_b32_e32 v209, 0xffff0000, v120
	v_lshlrev_b32_e32 v210, 16, v121
	v_and_b32_e32 v211, 0xffff0000, v121
	v_pk_fma_f32 v[208:209], v[224:225], v[240:241], v[208:209] op_sel_hi:[1,0,1]
	v_pk_fma_f32 v[210:211], v[226:227], v[240:241], v[210:211] op_sel_hi:[1,0,1]
	v_pk_fma_f32 v[208:209], v[228:229], v[242:243], v[208:209] op_sel_hi:[1,0,1]
	v_pk_fma_f32 v[210:211], v[230:231], v[242:243], v[210:211] op_sel_hi:[1,0,1]
	v_cvt_pk_f32_fp8_e32 v[232:233], v101
	v_cvt_pk_f32_fp8_sdwa v[234:235], v101 src0_sel:WORD_1
	v_cvt_pk_f32_fp8_e32 v[236:237], v109
	v_cvt_pk_f32_fp8_sdwa v[238:239], v109 src0_sel:WORD_1
	v_lshlrev_b32_e32 v212, 16, v122
	v_and_b32_e32 v213, 0xffff0000, v122
	v_lshlrev_b32_e32 v214, 16, v123
	v_and_b32_e32 v215, 0xffff0000, v123
	v_pk_fma_f32 v[212:213], v[232:233], v[240:241], v[212:213] op_sel_hi:[1,0,1]
	v_pk_fma_f32 v[214:215], v[234:235], v[240:241], v[214:215] op_sel_hi:[1,0,1]
	v_pk_fma_f32 v[212:213], v[236:237], v[242:243], v[212:213] op_sel_hi:[1,0,1]
	v_pk_fma_f32 v[214:215], v[238:239], v[242:243], v[214:215] op_sel_hi:[1,0,1]
	v_cvt_pk_f32_fp8_e32 v[224:225], v102
	v_cvt_pk_f32_fp8_sdwa v[226:227], v102 src0_sel:WORD_1
	v_cvt_pk_f32_fp8_e32 v[228:229], v110
	v_cvt_pk_f32_fp8_sdwa v[230:231], v110 src0_sel:WORD_1
	v_lshlrev_b32_e32 v216, 16, v124
	v_and_b32_e32 v217, 0xffff0000, v124
	v_lshlrev_b32_e32 v218, 16, v125
	v_and_b32_e32 v219, 0xffff0000, v125
	v_pk_fma_f32 v[216:217], v[224:225], v[240:241], v[216:217] op_sel_hi:[1,0,1]
	v_pk_fma_f32 v[218:219], v[226:227], v[240:241], v[218:219] op_sel_hi:[1,0,1]
	v_pk_fma_f32 v[216:217], v[228:229], v[242:243], v[216:217] op_sel_hi:[1,0,1]
	v_pk_fma_f32 v[218:219], v[230:231], v[242:243], v[218:219] op_sel_hi:[1,0,1]
	v_cvt_pk_f32_fp8_e32 v[232:233], v103
	v_cvt_pk_f32_fp8_sdwa v[234:235], v103 src0_sel:WORD_1
	v_cvt_pk_f32_fp8_e32 v[236:237], v111
	v_cvt_pk_f32_fp8_sdwa v[238:239], v111 src0_sel:WORD_1
	v_lshlrev_b32_e32 v220, 16, v126
	v_and_b32_e32 v221, 0xffff0000, v126
	v_lshlrev_b32_e32 v222, 16, v127
	v_and_b32_e32 v223, 0xffff0000, v127
	v_pk_fma_f32 v[220:221], v[232:233], v[240:241], v[220:221] op_sel_hi:[1,0,1]
	v_pk_fma_f32 v[222:223], v[234:235], v[240:241], v[222:223] op_sel_hi:[1,0,1]
	v_pk_fma_f32 v[220:221], v[236:237], v[242:243], v[220:221] op_sel_hi:[1,0,1]
	v_pk_fma_f32 v[222:223], v[238:239], v[242:243], v[222:223] op_sel_hi:[1,0,1]
	s_waitcnt vmcnt(55)
	s_add_u32 s56, s64, 0x1000000
	s_addc_u32 s57, s65, 0
	s_add_u32 s58, s56, 0x1000
	s_addc_u32 s59, s57, 0
	global_store_dwordx4 v4, v[192:195], s[56:57]
	global_store_dwordx4 v4, v[196:199], s[56:57] offset:1024
	global_store_dwordx4 v4, v[200:203], s[56:57] offset:2048
	global_store_dwordx4 v4, v[204:207], s[56:57] offset:3072
	global_store_dwordx4 v4, v[208:211], s[58:59]
	global_store_dwordx4 v4, v[212:215], s[58:59] offset:1024
	global_store_dwordx4 v4, v[216:219], s[58:59] offset:2048
	global_store_dwordx4 v4, v[220:223], s[58:59] offset:3072
	s_waitcnt vmcnt(32)
	s_lshl_b32 s50, s20, 11
	s_add_u32 s50, s48, s50
	s_addc_u32 s51, s49, 0
	s_lshl_b32 s52, s28, 11
	s_add_u32 s52, s48, s52
	s_addc_u32 s53, s49, 0
	s_add_u32 s54, s62, 0x2000000
	s_addc_u32 s55, s63, 0
	global_load_dword v96, v2, s[50:51]
	global_load_dword v97, v2, s[50:51] offset:256
	global_load_dword v98, v2, s[50:51] offset:512
	global_load_dword v99, v2, s[50:51] offset:768
	global_load_dword v100, v2, s[50:51] offset:1024
	global_load_dword v101, v2, s[50:51] offset:1280
	global_load_dword v102, v2, s[50:51] offset:1536
	global_load_dword v103, v2, s[50:51] offset:1792
	global_load_dword v104, v2, s[52:53]
	global_load_dword v105, v2, s[52:53] offset:256
	global_load_dword v106, v2, s[52:53] offset:512
	global_load_dword v107, v2, s[52:53] offset:768
	global_load_dword v108, v2, s[52:53] offset:1024
	global_load_dword v109, v2, s[52:53] offset:1280
	global_load_dword v110, v2, s[52:53] offset:1536
	global_load_dword v111, v2, s[52:53] offset:1792
	global_load_dwordx2 v[112:113], v3, s[54:55]
	global_load_dwordx2 v[114:115], v3, s[54:55] offset:512
	global_load_dwordx2 v[116:117], v3, s[54:55] offset:1024
	global_load_dwordx2 v[118:119], v3, s[54:55] offset:1536
	global_load_dwordx2 v[120:121], v3, s[54:55] offset:2048
	global_load_dwordx2 v[122:123], v3, s[54:55] offset:2560
	global_load_dwordx2 v[124:125], v3, s[54:55] offset:3072
	global_load_dwordx2 v[126:127], v3, s[54:55] offset:3584
	v_mov_b32_e32 v240, s34
	v_mov_b32_e32 v242, s42
	v_cvt_pk_f32_fp8_e32 v[224:225], v128
	v_cvt_pk_f32_fp8_sdwa v[226:227], v128 src0_sel:WORD_1
	v_cvt_pk_f32_fp8_e32 v[228:229], v136
	v_cvt_pk_f32_fp8_sdwa v[230:231], v136 src0_sel:WORD_1
	v_lshlrev_b32_e32 v192, 16, v144
	v_and_b32_e32 v193, 0xffff0000, v144
	v_lshlrev_b32_e32 v194, 16, v145
	v_and_b32_e32 v195, 0xffff0000, v145
	v_pk_fma_f32 v[192:193], v[224:225], v[240:241], v[192:193] op_sel_hi:[1,0,1]
	v_pk_fma_f32 v[194:195], v[226:227], v[240:241], v[194:195] op_sel_hi:[1,0,1]
	v_pk_fma_f32 v[192:193], v[228:229], v[242:243], v[192:193] op_sel_hi:[1,0,1]
	v_pk_fma_f32 v[194:195], v[230:231], v[242:243], v[194:195] op_sel_hi:[1,0,1]
	v_cvt_pk_f32_fp8_e32 v[232:233], v129
	v_cvt_pk_f32_fp8_sdwa v[234:235], v129 src0_sel:WORD_1
	v_cvt_pk_f32_fp8_e32 v[236:237], v137
	v_cvt_pk_f32_fp8_sdwa v[238:239], v137 src0_sel:WORD_1
	v_lshlrev_b32_e32 v196, 16, v146
	v_and_b32_e32 v197, 0xffff0000, v146
	v_lshlrev_b32_e32 v198, 16, v147
	v_and_b32_e32 v199, 0xffff0000, v147
	v_pk_fma_f32 v[196:197], v[232:233], v[240:241], v[196:197] op_sel_hi:[1,0,1]
	v_pk_fma_f32 v[198:199], v[234:235], v[240:241], v[198:199] op_sel_hi:[1,0,1]
	v_pk_fma_f32 v[196:197], v[236:237], v[242:243], v[196:197] op_sel_hi:[1,0,1]
	v_pk_fma_f32 v[198:199], v[238:239], v[242:243], v[198:199] op_sel_hi:[1,0,1]
	v_cvt_pk_f32_fp8_e32 v[224:225], v130
	v_cvt_pk_f32_fp8_sdwa v[226:227], v130 src0_sel:WORD_1
	v_cvt_pk_f32_fp8_e32 v[228:229], v138
	v_cvt_pk_f32_fp8_sdwa v[230:231], v138 src0_sel:WORD_1
	v_lshlrev_b32_e32 v200, 16, v148
	v_and_b32_e32 v201, 0xffff0000, v148
	v_lshlrev_b32_e32 v202, 16, v149
	v_and_b32_e32 v203, 0xffff0000, v149
	v_pk_fma_f32 v[200:201], v[224:225], v[240:241], v[200:201] op_sel_hi:[1,0,1]
	v_pk_fma_f32 v[202:203], v[226:227], v[240:241], v[202:203] op_sel_hi:[1,0,1]
	v_pk_fma_f32 v[200:201], v[228:229], v[242:243], v[200:201] op_sel_hi:[1,0,1]
	v_pk_fma_f32 v[202:203], v[230:231], v[242:243], v[202:203] op_sel_hi:[1,0,1]
	v_cvt_pk_f32_fp8_e32 v[232:233], v131
	v_cvt_pk_f32_fp8_sdwa v[234:235], v131 src0_sel:WORD_1
	v_cvt_pk_f32_fp8_e32 v[236:237], v139
	v_cvt_pk_f32_fp8_sdwa v[238:239], v139 src0_sel:WORD_1
	v_lshlrev_b32_e32 v204, 16, v150
	v_and_b32_e32 v205, 0xffff0000, v150
	v_lshlrev_b32_e32 v206, 16, v151
	v_and_b32_e32 v207, 0xffff0000, v151
	v_pk_fma_f32 v[204:205], v[232:233], v[240:241], v[204:205] op_sel_hi:[1,0,1]
	v_pk_fma_f32 v[206:207], v[234:235], v[240:241], v[206:207] op_sel_hi:[1,0,1]
	v_pk_fma_f32 v[204:205], v[236:237], v[242:243], v[204:205] op_sel_hi:[1,0,1]
	v_pk_fma_f32 v[206:207], v[238:239], v[242:243], v[206:207] op_sel_hi:[1,0,1]
	v_cvt_pk_f32_fp8_e32 v[224:225], v132
	v_cvt_pk_f32_fp8_sdwa v[226:227], v132 src0_sel:WORD_1
	v_cvt_pk_f32_fp8_e32 v[228:229], v140
	v_cvt_pk_f32_fp8_sdwa v[230:231], v140 src0_sel:WORD_1
	v_lshlrev_b32_e32 v208, 16, v152
	v_and_b32_e32 v209, 0xffff0000, v152
	v_lshlrev_b32_e32 v210, 16, v153
	v_and_b32_e32 v211, 0xffff0000, v153
	v_pk_fma_f32 v[208:209], v[224:225], v[240:241], v[208:209] op_sel_hi:[1,0,1]
	v_pk_fma_f32 v[210:211], v[226:227], v[240:241], v[210:211] op_sel_hi:[1,0,1]
	v_pk_fma_f32 v[208:209], v[228:229], v[242:243], v[208:209] op_sel_hi:[1,0,1]
	v_pk_fma_f32 v[210:211], v[230:231], v[242:243], v[210:211] op_sel_hi:[1,0,1]
	v_cvt_pk_f32_fp8_e32 v[232:233], v133
	v_cvt_pk_f32_fp8_sdwa v[234:235], v133 src0_sel:WORD_1
	v_cvt_pk_f32_fp8_e32 v[236:237], v141
	v_cvt_pk_f32_fp8_sdwa v[238:239], v141 src0_sel:WORD_1
	v_lshlrev_b32_e32 v212, 16, v154
	v_and_b32_e32 v213, 0xffff0000, v154
	v_lshlrev_b32_e32 v214, 16, v155
	v_and_b32_e32 v215, 0xffff0000, v155
	v_pk_fma_f32 v[212:213], v[232:233], v[240:241], v[212:213] op_sel_hi:[1,0,1]
	v_pk_fma_f32 v[214:215], v[234:235], v[240:241], v[214:215] op_sel_hi:[1,0,1]
	v_pk_fma_f32 v[212:213], v[236:237], v[242:243], v[212:213] op_sel_hi:[1,0,1]
	v_pk_fma_f32 v[214:215], v[238:239], v[242:243], v[214:215] op_sel_hi:[1,0,1]
	v_cvt_pk_f32_fp8_e32 v[224:225], v134
	v_cvt_pk_f32_fp8_sdwa v[226:227], v134 src0_sel:WORD_1
	v_cvt_pk_f32_fp8_e32 v[228:229], v142
	v_cvt_pk_f32_fp8_sdwa v[230:231], v142 src0_sel:WORD_1
	v_lshlrev_b32_e32 v216, 16, v156
	v_and_b32_e32 v217, 0xffff0000, v156
	v_lshlrev_b32_e32 v218, 16, v157
	v_and_b32_e32 v219, 0xffff0000, v157
	v_pk_fma_f32 v[216:217], v[224:225], v[240:241], v[216:217] op_sel_hi:[1,0,1]
	v_pk_fma_f32 v[218:219], v[226:227], v[240:241], v[218:219] op_sel_hi:[1,0,1]
	v_pk_fma_f32 v[216:217], v[228:229], v[242:243], v[216:217] op_sel_hi:[1,0,1]
	v_pk_fma_f32 v[218:219], v[230:231], v[242:243], v[218:219] op_sel_hi:[1,0,1]
	v_cvt_pk_f32_fp8_e32 v[232:233], v135
	v_cvt_pk_f32_fp8_sdwa v[234:235], v135 src0_sel:WORD_1
	v_cvt_pk_f32_fp8_e32 v[236:237], v143
	v_cvt_pk_f32_fp8_sdwa v[238:239], v143 src0_sel:WORD_1
	v_lshlrev_b32_e32 v220, 16, v158
	v_and_b32_e32 v221, 0xffff0000, v158
	v_lshlrev_b32_e32 v222, 16, v159
	v_and_b32_e32 v223, 0xffff0000, v159
	v_pk_fma_f32 v[220:221], v[232:233], v[240:241], v[220:221] op_sel_hi:[1,0,1]
	v_pk_fma_f32 v[222:223], v[234:235], v[240:241], v[222:223] op_sel_hi:[1,0,1]
	v_pk_fma_f32 v[220:221], v[236:237], v[242:243], v[220:221] op_sel_hi:[1,0,1]
	v_pk_fma_f32 v[222:223], v[238:239], v[242:243], v[222:223] op_sel_hi:[1,0,1]
	s_waitcnt vmcnt(55)
	s_add_u32 s56, s64, 0x2000000
	s_addc_u32 s57, s65, 0
	s_add_u32 s58, s56, 0x1000
	s_addc_u32 s59, s57, 0
	global_store_dwordx4 v4, v[192:195], s[56:57]
	global_store_dwordx4 v4, v[196:199], s[56:57] offset:1024
	global_store_dwordx4 v4, v[200:203], s[56:57] offset:2048
	global_store_dwordx4 v4, v[204:207], s[56:57] offset:3072
	global_store_dwordx4 v4, v[208:211], s[58:59]
	global_store_dwordx4 v4, v[212:215], s[58:59] offset:1024
	global_store_dwordx4 v4, v[216:219], s[58:59] offset:2048
	global_store_dwordx4 v4, v[220:223], s[58:59] offset:3072
	s_waitcnt vmcnt(32)
	s_lshl_b32 s50, s21, 11
	s_add_u32 s50, s48, s50
	s_addc_u32 s51, s49, 0
	s_lshl_b32 s52, s29, 11
	s_add_u32 s52, s48, s52
	s_addc_u32 s53, s49, 0
	s_add_u32 s54, s62, 0x2800000
	s_addc_u32 s55, s63, 0
	global_load_dword v128, v2, s[50:51]
	global_load_dword v129, v2, s[50:51] offset:256
	global_load_dword v130, v2, s[50:51] offset:512
	global_load_dword v131, v2, s[50:51] offset:768
	global_load_dword v132, v2, s[50:51] offset:1024
	global_load_dword v133, v2, s[50:51] offset:1280
	global_load_dword v134, v2, s[50:51] offset:1536
	global_load_dword v135, v2, s[50:51] offset:1792
	global_load_dword v136, v2, s[52:53]
	global_load_dword v137, v2, s[52:53] offset:256
	global_load_dword v138, v2, s[52:53] offset:512
	global_load_dword v139, v2, s[52:53] offset:768
	global_load_dword v140, v2, s[52:53] offset:1024
	global_load_dword v141, v2, s[52:53] offset:1280
	global_load_dword v142, v2, s[52:53] offset:1536
	global_load_dword v143, v2, s[52:53] offset:1792
	global_load_dwordx2 v[144:145], v3, s[54:55]
	global_load_dwordx2 v[146:147], v3, s[54:55] offset:512
	global_load_dwordx2 v[148:149], v3, s[54:55] offset:1024
	global_load_dwordx2 v[150:151], v3, s[54:55] offset:1536
	global_load_dwordx2 v[152:153], v3, s[54:55] offset:2048
	global_load_dwordx2 v[154:155], v3, s[54:55] offset:2560
	global_load_dwordx2 v[156:157], v3, s[54:55] offset:3072
	global_load_dwordx2 v[158:159], v3, s[54:55] offset:3584
	v_mov_b32_e32 v240, s35
	v_mov_b32_e32 v242, s43
	v_cvt_pk_f32_fp8_e32 v[224:225], v64
	v_cvt_pk_f32_fp8_sdwa v[226:227], v64 src0_sel:WORD_1
	v_cvt_pk_f32_fp8_e32 v[228:229], v72
	v_cvt_pk_f32_fp8_sdwa v[230:231], v72 src0_sel:WORD_1
	v_lshlrev_b32_e32 v192, 16, v80
	v_and_b32_e32 v193, 0xffff0000, v80
	v_lshlrev_b32_e32 v194, 16, v81
	v_and_b32_e32 v195, 0xffff0000, v81
	v_pk_fma_f32 v[192:193], v[224:225], v[240:241], v[192:193] op_sel_hi:[1,0,1]
	v_pk_fma_f32 v[194:195], v[226:227], v[240:241], v[194:195] op_sel_hi:[1,0,1]
	v_pk_fma_f32 v[192:193], v[228:229], v[242:243], v[192:193] op_sel_hi:[1,0,1]
	v_pk_fma_f32 v[194:195], v[230:231], v[242:243], v[194:195] op_sel_hi:[1,0,1]
	v_cvt_pk_f32_fp8_e32 v[232:233], v65
	v_cvt_pk_f32_fp8_sdwa v[234:235], v65 src0_sel:WORD_1
	v_cvt_pk_f32_fp8_e32 v[236:237], v73
	v_cvt_pk_f32_fp8_sdwa v[238:239], v73 src0_sel:WORD_1
	v_lshlrev_b32_e32 v196, 16, v82
	v_and_b32_e32 v197, 0xffff0000, v82
	v_lshlrev_b32_e32 v198, 16, v83
	v_and_b32_e32 v199, 0xffff0000, v83
	v_pk_fma_f32 v[196:197], v[232:233], v[240:241], v[196:197] op_sel_hi:[1,0,1]
	v_pk_fma_f32 v[198:199], v[234:235], v[240:241], v[198:199] op_sel_hi:[1,0,1]
	v_pk_fma_f32 v[196:197], v[236:237], v[242:243], v[196:197] op_sel_hi:[1,0,1]
	v_pk_fma_f32 v[198:199], v[238:239], v[242:243], v[198:199] op_sel_hi:[1,0,1]
	v_cvt_pk_f32_fp8_e32 v[224:225], v66
	v_cvt_pk_f32_fp8_sdwa v[226:227], v66 src0_sel:WORD_1
	v_cvt_pk_f32_fp8_e32 v[228:229], v74
	v_cvt_pk_f32_fp8_sdwa v[230:231], v74 src0_sel:WORD_1
	v_lshlrev_b32_e32 v200, 16, v84
	v_and_b32_e32 v201, 0xffff0000, v84
	v_lshlrev_b32_e32 v202, 16, v85
	v_and_b32_e32 v203, 0xffff0000, v85
	v_pk_fma_f32 v[200:201], v[224:225], v[240:241], v[200:201] op_sel_hi:[1,0,1]
	v_pk_fma_f32 v[202:203], v[226:227], v[240:241], v[202:203] op_sel_hi:[1,0,1]
	v_pk_fma_f32 v[200:201], v[228:229], v[242:243], v[200:201] op_sel_hi:[1,0,1]
	v_pk_fma_f32 v[202:203], v[230:231], v[242:243], v[202:203] op_sel_hi:[1,0,1]
	v_cvt_pk_f32_fp8_e32 v[232:233], v67
	v_cvt_pk_f32_fp8_sdwa v[234:235], v67 src0_sel:WORD_1
	v_cvt_pk_f32_fp8_e32 v[236:237], v75
	v_cvt_pk_f32_fp8_sdwa v[238:239], v75 src0_sel:WORD_1
	v_lshlrev_b32_e32 v204, 16, v86
	v_and_b32_e32 v205, 0xffff0000, v86
	v_lshlrev_b32_e32 v206, 16, v87
	v_and_b32_e32 v207, 0xffff0000, v87
	v_pk_fma_f32 v[204:205], v[232:233], v[240:241], v[204:205] op_sel_hi:[1,0,1]
	v_pk_fma_f32 v[206:207], v[234:235], v[240:241], v[206:207] op_sel_hi:[1,0,1]
	v_pk_fma_f32 v[204:205], v[236:237], v[242:243], v[204:205] op_sel_hi:[1,0,1]
	v_pk_fma_f32 v[206:207], v[238:239], v[242:243], v[206:207] op_sel_hi:[1,0,1]
	v_cvt_pk_f32_fp8_e32 v[224:225], v68
	v_cvt_pk_f32_fp8_sdwa v[226:227], v68 src0_sel:WORD_1
	v_cvt_pk_f32_fp8_e32 v[228:229], v76
	v_cvt_pk_f32_fp8_sdwa v[230:231], v76 src0_sel:WORD_1
	v_lshlrev_b32_e32 v208, 16, v88
	v_and_b32_e32 v209, 0xffff0000, v88
	v_lshlrev_b32_e32 v210, 16, v89
	v_and_b32_e32 v211, 0xffff0000, v89
	v_pk_fma_f32 v[208:209], v[224:225], v[240:241], v[208:209] op_sel_hi:[1,0,1]
	v_pk_fma_f32 v[210:211], v[226:227], v[240:241], v[210:211] op_sel_hi:[1,0,1]
	v_pk_fma_f32 v[208:209], v[228:229], v[242:243], v[208:209] op_sel_hi:[1,0,1]
	v_pk_fma_f32 v[210:211], v[230:231], v[242:243], v[210:211] op_sel_hi:[1,0,1]
	v_cvt_pk_f32_fp8_e32 v[232:233], v69
	v_cvt_pk_f32_fp8_sdwa v[234:235], v69 src0_sel:WORD_1
	v_cvt_pk_f32_fp8_e32 v[236:237], v77
	v_cvt_pk_f32_fp8_sdwa v[238:239], v77 src0_sel:WORD_1
	v_lshlrev_b32_e32 v212, 16, v90
	v_and_b32_e32 v213, 0xffff0000, v90
	v_lshlrev_b32_e32 v214, 16, v91
	v_and_b32_e32 v215, 0xffff0000, v91
	v_pk_fma_f32 v[212:213], v[232:233], v[240:241], v[212:213] op_sel_hi:[1,0,1]
	v_pk_fma_f32 v[214:215], v[234:235], v[240:241], v[214:215] op_sel_hi:[1,0,1]
	v_pk_fma_f32 v[212:213], v[236:237], v[242:243], v[212:213] op_sel_hi:[1,0,1]
	v_pk_fma_f32 v[214:215], v[238:239], v[242:243], v[214:215] op_sel_hi:[1,0,1]
	v_cvt_pk_f32_fp8_e32 v[224:225], v70
	v_cvt_pk_f32_fp8_sdwa v[226:227], v70 src0_sel:WORD_1
	v_cvt_pk_f32_fp8_e32 v[228:229], v78
	v_cvt_pk_f32_fp8_sdwa v[230:231], v78 src0_sel:WORD_1
	v_lshlrev_b32_e32 v216, 16, v92
	v_and_b32_e32 v217, 0xffff0000, v92
	v_lshlrev_b32_e32 v218, 16, v93
	v_and_b32_e32 v219, 0xffff0000, v93
	v_pk_fma_f32 v[216:217], v[224:225], v[240:241], v[216:217] op_sel_hi:[1,0,1]
	v_pk_fma_f32 v[218:219], v[226:227], v[240:241], v[218:219] op_sel_hi:[1,0,1]
	v_pk_fma_f32 v[216:217], v[228:229], v[242:243], v[216:217] op_sel_hi:[1,0,1]
	v_pk_fma_f32 v[218:219], v[230:231], v[242:243], v[218:219] op_sel_hi:[1,0,1]
	v_cvt_pk_f32_fp8_e32 v[232:233], v71
	v_cvt_pk_f32_fp8_sdwa v[234:235], v71 src0_sel:WORD_1
	v_cvt_pk_f32_fp8_e32 v[236:237], v79
	v_cvt_pk_f32_fp8_sdwa v[238:239], v79 src0_sel:WORD_1
	v_lshlrev_b32_e32 v220, 16, v94
	v_and_b32_e32 v221, 0xffff0000, v94
	v_lshlrev_b32_e32 v222, 16, v95
	v_and_b32_e32 v223, 0xffff0000, v95
	v_pk_fma_f32 v[220:221], v[232:233], v[240:241], v[220:221] op_sel_hi:[1,0,1]
	v_pk_fma_f32 v[222:223], v[234:235], v[240:241], v[222:223] op_sel_hi:[1,0,1]
	v_pk_fma_f32 v[220:221], v[236:237], v[242:243], v[220:221] op_sel_hi:[1,0,1]
	v_pk_fma_f32 v[222:223], v[238:239], v[242:243], v[222:223] op_sel_hi:[1,0,1]
	s_waitcnt vmcnt(55)
	s_add_u32 s56, s64, 0x3000000
	s_addc_u32 s57, s65, 0
	s_add_u32 s58, s56, 0x1000
	s_addc_u32 s59, s57, 0
	global_store_dwordx4 v4, v[192:195], s[56:57]
	global_store_dwordx4 v4, v[196:199], s[56:57] offset:1024
	global_store_dwordx4 v4, v[200:203], s[56:57] offset:2048
	global_store_dwordx4 v4, v[204:207], s[56:57] offset:3072
	global_store_dwordx4 v4, v[208:211], s[58:59]
	global_store_dwordx4 v4, v[212:215], s[58:59] offset:1024
	global_store_dwordx4 v4, v[216:219], s[58:59] offset:2048
	global_store_dwordx4 v4, v[220:223], s[58:59] offset:3072
	s_waitcnt vmcnt(32)
	s_lshl_b32 s50, s22, 11
	s_add_u32 s50, s48, s50
	s_addc_u32 s51, s49, 0
	s_lshl_b32 s52, s30, 11
	s_add_u32 s52, s48, s52
	s_addc_u32 s53, s49, 0
	s_add_u32 s54, s62, 0x3000000
	s_addc_u32 s55, s63, 0
	global_load_dword v64, v2, s[50:51]
	global_load_dword v65, v2, s[50:51] offset:256
	global_load_dword v66, v2, s[50:51] offset:512
	global_load_dword v67, v2, s[50:51] offset:768
	global_load_dword v68, v2, s[50:51] offset:1024
	global_load_dword v69, v2, s[50:51] offset:1280
	global_load_dword v70, v2, s[50:51] offset:1536
	global_load_dword v71, v2, s[50:51] offset:1792
	global_load_dword v72, v2, s[52:53]
	global_load_dword v73, v2, s[52:53] offset:256
	global_load_dword v74, v2, s[52:53] offset:512
	global_load_dword v75, v2, s[52:53] offset:768
	global_load_dword v76, v2, s[52:53] offset:1024
	global_load_dword v77, v2, s[52:53] offset:1280
	global_load_dword v78, v2, s[52:53] offset:1536
	global_load_dword v79, v2, s[52:53] offset:1792
	global_load_dwordx2 v[80:81], v3, s[54:55]
	global_load_dwordx2 v[82:83], v3, s[54:55] offset:512
	global_load_dwordx2 v[84:85], v3, s[54:55] offset:1024
	global_load_dwordx2 v[86:87], v3, s[54:55] offset:1536
	global_load_dwordx2 v[88:89], v3, s[54:55] offset:2048
	global_load_dwordx2 v[90:91], v3, s[54:55] offset:2560
	global_load_dwordx2 v[92:93], v3, s[54:55] offset:3072
	global_load_dwordx2 v[94:95], v3, s[54:55] offset:3584
	v_mov_b32_e32 v240, s36
	v_mov_b32_e32 v242, s44
	v_cvt_pk_f32_fp8_e32 v[224:225], v96
	v_cvt_pk_f32_fp8_sdwa v[226:227], v96 src0_sel:WORD_1
	v_cvt_pk_f32_fp8_e32 v[228:229], v104
	v_cvt_pk_f32_fp8_sdwa v[230:231], v104 src0_sel:WORD_1
	v_lshlrev_b32_e32 v192, 16, v112
	v_and_b32_e32 v193, 0xffff0000, v112
	v_lshlrev_b32_e32 v194, 16, v113
	v_and_b32_e32 v195, 0xffff0000, v113
	v_pk_fma_f32 v[192:193], v[224:225], v[240:241], v[192:193] op_sel_hi:[1,0,1]
	v_pk_fma_f32 v[194:195], v[226:227], v[240:241], v[194:195] op_sel_hi:[1,0,1]
	v_pk_fma_f32 v[192:193], v[228:229], v[242:243], v[192:193] op_sel_hi:[1,0,1]
	v_pk_fma_f32 v[194:195], v[230:231], v[242:243], v[194:195] op_sel_hi:[1,0,1]
	v_cvt_pk_f32_fp8_e32 v[232:233], v97
	v_cvt_pk_f32_fp8_sdwa v[234:235], v97 src0_sel:WORD_1
	v_cvt_pk_f32_fp8_e32 v[236:237], v105
	v_cvt_pk_f32_fp8_sdwa v[238:239], v105 src0_sel:WORD_1
	v_lshlrev_b32_e32 v196, 16, v114
	v_and_b32_e32 v197, 0xffff0000, v114
	v_lshlrev_b32_e32 v198, 16, v115
	v_and_b32_e32 v199, 0xffff0000, v115
	v_pk_fma_f32 v[196:197], v[232:233], v[240:241], v[196:197] op_sel_hi:[1,0,1]
	v_pk_fma_f32 v[198:199], v[234:235], v[240:241], v[198:199] op_sel_hi:[1,0,1]
	v_pk_fma_f32 v[196:197], v[236:237], v[242:243], v[196:197] op_sel_hi:[1,0,1]
	v_pk_fma_f32 v[198:199], v[238:239], v[242:243], v[198:199] op_sel_hi:[1,0,1]
	v_cvt_pk_f32_fp8_e32 v[224:225], v98
	v_cvt_pk_f32_fp8_sdwa v[226:227], v98 src0_sel:WORD_1
	v_cvt_pk_f32_fp8_e32 v[228:229], v106
	v_cvt_pk_f32_fp8_sdwa v[230:231], v106 src0_sel:WORD_1
	v_lshlrev_b32_e32 v200, 16, v116
	v_and_b32_e32 v201, 0xffff0000, v116
	v_lshlrev_b32_e32 v202, 16, v117
	v_and_b32_e32 v203, 0xffff0000, v117
	v_pk_fma_f32 v[200:201], v[224:225], v[240:241], v[200:201] op_sel_hi:[1,0,1]
	v_pk_fma_f32 v[202:203], v[226:227], v[240:241], v[202:203] op_sel_hi:[1,0,1]
	v_pk_fma_f32 v[200:201], v[228:229], v[242:243], v[200:201] op_sel_hi:[1,0,1]
	v_pk_fma_f32 v[202:203], v[230:231], v[242:243], v[202:203] op_sel_hi:[1,0,1]
	v_cvt_pk_f32_fp8_e32 v[232:233], v99
	v_cvt_pk_f32_fp8_sdwa v[234:235], v99 src0_sel:WORD_1
	v_cvt_pk_f32_fp8_e32 v[236:237], v107
	v_cvt_pk_f32_fp8_sdwa v[238:239], v107 src0_sel:WORD_1
	v_lshlrev_b32_e32 v204, 16, v118
	v_and_b32_e32 v205, 0xffff0000, v118
	v_lshlrev_b32_e32 v206, 16, v119
	v_and_b32_e32 v207, 0xffff0000, v119
	v_pk_fma_f32 v[204:205], v[232:233], v[240:241], v[204:205] op_sel_hi:[1,0,1]
	v_pk_fma_f32 v[206:207], v[234:235], v[240:241], v[206:207] op_sel_hi:[1,0,1]
	v_pk_fma_f32 v[204:205], v[236:237], v[242:243], v[204:205] op_sel_hi:[1,0,1]
	v_pk_fma_f32 v[206:207], v[238:239], v[242:243], v[206:207] op_sel_hi:[1,0,1]
	v_cvt_pk_f32_fp8_e32 v[224:225], v100
	v_cvt_pk_f32_fp8_sdwa v[226:227], v100 src0_sel:WORD_1
	v_cvt_pk_f32_fp8_e32 v[228:229], v108
	v_cvt_pk_f32_fp8_sdwa v[230:231], v108 src0_sel:WORD_1
	v_lshlrev_b32_e32 v208, 16, v120
	v_and_b32_e32 v209, 0xffff0000, v120
	v_lshlrev_b32_e32 v210, 16, v121
	v_and_b32_e32 v211, 0xffff0000, v121
	v_pk_fma_f32 v[208:209], v[224:225], v[240:241], v[208:209] op_sel_hi:[1,0,1]
	v_pk_fma_f32 v[210:211], v[226:227], v[240:241], v[210:211] op_sel_hi:[1,0,1]
	v_pk_fma_f32 v[208:209], v[228:229], v[242:243], v[208:209] op_sel_hi:[1,0,1]
	v_pk_fma_f32 v[210:211], v[230:231], v[242:243], v[210:211] op_sel_hi:[1,0,1]
	v_cvt_pk_f32_fp8_e32 v[232:233], v101
	v_cvt_pk_f32_fp8_sdwa v[234:235], v101 src0_sel:WORD_1
	v_cvt_pk_f32_fp8_e32 v[236:237], v109
	v_cvt_pk_f32_fp8_sdwa v[238:239], v109 src0_sel:WORD_1
	v_lshlrev_b32_e32 v212, 16, v122
	v_and_b32_e32 v213, 0xffff0000, v122
	v_lshlrev_b32_e32 v214, 16, v123
	v_and_b32_e32 v215, 0xffff0000, v123
	v_pk_fma_f32 v[212:213], v[232:233], v[240:241], v[212:213] op_sel_hi:[1,0,1]
	v_pk_fma_f32 v[214:215], v[234:235], v[240:241], v[214:215] op_sel_hi:[1,0,1]
	v_pk_fma_f32 v[212:213], v[236:237], v[242:243], v[212:213] op_sel_hi:[1,0,1]
	v_pk_fma_f32 v[214:215], v[238:239], v[242:243], v[214:215] op_sel_hi:[1,0,1]
	v_cvt_pk_f32_fp8_e32 v[224:225], v102
	v_cvt_pk_f32_fp8_sdwa v[226:227], v102 src0_sel:WORD_1
	v_cvt_pk_f32_fp8_e32 v[228:229], v110
	v_cvt_pk_f32_fp8_sdwa v[230:231], v110 src0_sel:WORD_1
	v_lshlrev_b32_e32 v216, 16, v124
	v_and_b32_e32 v217, 0xffff0000, v124
	v_lshlrev_b32_e32 v218, 16, v125
	v_and_b32_e32 v219, 0xffff0000, v125
	v_pk_fma_f32 v[216:217], v[224:225], v[240:241], v[216:217] op_sel_hi:[1,0,1]
	v_pk_fma_f32 v[218:219], v[226:227], v[240:241], v[218:219] op_sel_hi:[1,0,1]
	v_pk_fma_f32 v[216:217], v[228:229], v[242:243], v[216:217] op_sel_hi:[1,0,1]
	v_pk_fma_f32 v[218:219], v[230:231], v[242:243], v[218:219] op_sel_hi:[1,0,1]
	v_cvt_pk_f32_fp8_e32 v[232:233], v103
	v_cvt_pk_f32_fp8_sdwa v[234:235], v103 src0_sel:WORD_1
	v_cvt_pk_f32_fp8_e32 v[236:237], v111
	v_cvt_pk_f32_fp8_sdwa v[238:239], v111 src0_sel:WORD_1
	v_lshlrev_b32_e32 v220, 16, v126
	v_and_b32_e32 v221, 0xffff0000, v126
	v_lshlrev_b32_e32 v222, 16, v127
	v_and_b32_e32 v223, 0xffff0000, v127
	v_pk_fma_f32 v[220:221], v[232:233], v[240:241], v[220:221] op_sel_hi:[1,0,1]
	v_pk_fma_f32 v[222:223], v[234:235], v[240:241], v[222:223] op_sel_hi:[1,0,1]
	v_pk_fma_f32 v[220:221], v[236:237], v[242:243], v[220:221] op_sel_hi:[1,0,1]
	v_pk_fma_f32 v[222:223], v[238:239], v[242:243], v[222:223] op_sel_hi:[1,0,1]
	s_waitcnt vmcnt(55)
	s_add_u32 s56, s64, 0x4000000
	s_addc_u32 s57, s65, 0
	s_add_u32 s58, s56, 0x1000
	s_addc_u32 s59, s57, 0
	global_store_dwordx4 v4, v[192:195], s[56:57]
	global_store_dwordx4 v4, v[196:199], s[56:57] offset:1024
	global_store_dwordx4 v4, v[200:203], s[56:57] offset:2048
	global_store_dwordx4 v4, v[204:207], s[56:57] offset:3072
	global_store_dwordx4 v4, v[208:211], s[58:59]
	global_store_dwordx4 v4, v[212:215], s[58:59] offset:1024
	global_store_dwordx4 v4, v[216:219], s[58:59] offset:2048
	global_store_dwordx4 v4, v[220:223], s[58:59] offset:3072
	s_waitcnt vmcnt(32)
	s_lshl_b32 s50, s23, 11
	s_add_u32 s50, s48, s50
	s_addc_u32 s51, s49, 0
	s_lshl_b32 s52, s31, 11
	s_add_u32 s52, s48, s52
	s_addc_u32 s53, s49, 0
	s_add_u32 s54, s62, 0x3800000
	s_addc_u32 s55, s63, 0
	global_load_dword v96, v2, s[50:51]
	global_load_dword v97, v2, s[50:51] offset:256
	global_load_dword v98, v2, s[50:51] offset:512
	global_load_dword v99, v2, s[50:51] offset:768
	global_load_dword v100, v2, s[50:51] offset:1024
	global_load_dword v101, v2, s[50:51] offset:1280
	global_load_dword v102, v2, s[50:51] offset:1536
	global_load_dword v103, v2, s[50:51] offset:1792
	global_load_dword v104, v2, s[52:53]
	global_load_dword v105, v2, s[52:53] offset:256
	global_load_dword v106, v2, s[52:53] offset:512
	global_load_dword v107, v2, s[52:53] offset:768
	global_load_dword v108, v2, s[52:53] offset:1024
	global_load_dword v109, v2, s[52:53] offset:1280
	global_load_dword v110, v2, s[52:53] offset:1536
	global_load_dword v111, v2, s[52:53] offset:1792
	global_load_dwordx2 v[112:113], v3, s[54:55]
	global_load_dwordx2 v[114:115], v3, s[54:55] offset:512
	global_load_dwordx2 v[116:117], v3, s[54:55] offset:1024
	global_load_dwordx2 v[118:119], v3, s[54:55] offset:1536
	global_load_dwordx2 v[120:121], v3, s[54:55] offset:2048
	global_load_dwordx2 v[122:123], v3, s[54:55] offset:2560
	global_load_dwordx2 v[124:125], v3, s[54:55] offset:3072
	global_load_dwordx2 v[126:127], v3, s[54:55] offset:3584
	v_mov_b32_e32 v240, s37
	v_mov_b32_e32 v242, s45
	v_cvt_pk_f32_fp8_e32 v[224:225], v128
	v_cvt_pk_f32_fp8_sdwa v[226:227], v128 src0_sel:WORD_1
	v_cvt_pk_f32_fp8_e32 v[228:229], v136
	v_cvt_pk_f32_fp8_sdwa v[230:231], v136 src0_sel:WORD_1
	v_lshlrev_b32_e32 v192, 16, v144
	v_and_b32_e32 v193, 0xffff0000, v144
	v_lshlrev_b32_e32 v194, 16, v145
	v_and_b32_e32 v195, 0xffff0000, v145
	v_pk_fma_f32 v[192:193], v[224:225], v[240:241], v[192:193] op_sel_hi:[1,0,1]
	v_pk_fma_f32 v[194:195], v[226:227], v[240:241], v[194:195] op_sel_hi:[1,0,1]
	v_pk_fma_f32 v[192:193], v[228:229], v[242:243], v[192:193] op_sel_hi:[1,0,1]
	v_pk_fma_f32 v[194:195], v[230:231], v[242:243], v[194:195] op_sel_hi:[1,0,1]
	v_cvt_pk_f32_fp8_e32 v[232:233], v129
	v_cvt_pk_f32_fp8_sdwa v[234:235], v129 src0_sel:WORD_1
	v_cvt_pk_f32_fp8_e32 v[236:237], v137
	v_cvt_pk_f32_fp8_sdwa v[238:239], v137 src0_sel:WORD_1
	v_lshlrev_b32_e32 v196, 16, v146
	v_and_b32_e32 v197, 0xffff0000, v146
	v_lshlrev_b32_e32 v198, 16, v147
	v_and_b32_e32 v199, 0xffff0000, v147
	v_pk_fma_f32 v[196:197], v[232:233], v[240:241], v[196:197] op_sel_hi:[1,0,1]
	v_pk_fma_f32 v[198:199], v[234:235], v[240:241], v[198:199] op_sel_hi:[1,0,1]
	v_pk_fma_f32 v[196:197], v[236:237], v[242:243], v[196:197] op_sel_hi:[1,0,1]
	v_pk_fma_f32 v[198:199], v[238:239], v[242:243], v[198:199] op_sel_hi:[1,0,1]
	v_cvt_pk_f32_fp8_e32 v[224:225], v130
	v_cvt_pk_f32_fp8_sdwa v[226:227], v130 src0_sel:WORD_1
	v_cvt_pk_f32_fp8_e32 v[228:229], v138
	v_cvt_pk_f32_fp8_sdwa v[230:231], v138 src0_sel:WORD_1
	v_lshlrev_b32_e32 v200, 16, v148
	v_and_b32_e32 v201, 0xffff0000, v148
	v_lshlrev_b32_e32 v202, 16, v149
	v_and_b32_e32 v203, 0xffff0000, v149
	v_pk_fma_f32 v[200:201], v[224:225], v[240:241], v[200:201] op_sel_hi:[1,0,1]
	v_pk_fma_f32 v[202:203], v[226:227], v[240:241], v[202:203] op_sel_hi:[1,0,1]
	v_pk_fma_f32 v[200:201], v[228:229], v[242:243], v[200:201] op_sel_hi:[1,0,1]
	v_pk_fma_f32 v[202:203], v[230:231], v[242:243], v[202:203] op_sel_hi:[1,0,1]
	v_cvt_pk_f32_fp8_e32 v[232:233], v131
	v_cvt_pk_f32_fp8_sdwa v[234:235], v131 src0_sel:WORD_1
	v_cvt_pk_f32_fp8_e32 v[236:237], v139
	v_cvt_pk_f32_fp8_sdwa v[238:239], v139 src0_sel:WORD_1
	v_lshlrev_b32_e32 v204, 16, v150
	v_and_b32_e32 v205, 0xffff0000, v150
	v_lshlrev_b32_e32 v206, 16, v151
	v_and_b32_e32 v207, 0xffff0000, v151
	v_pk_fma_f32 v[204:205], v[232:233], v[240:241], v[204:205] op_sel_hi:[1,0,1]
	v_pk_fma_f32 v[206:207], v[234:235], v[240:241], v[206:207] op_sel_hi:[1,0,1]
	v_pk_fma_f32 v[204:205], v[236:237], v[242:243], v[204:205] op_sel_hi:[1,0,1]
	v_pk_fma_f32 v[206:207], v[238:239], v[242:243], v[206:207] op_sel_hi:[1,0,1]
	v_cvt_pk_f32_fp8_e32 v[224:225], v132
	v_cvt_pk_f32_fp8_sdwa v[226:227], v132 src0_sel:WORD_1
	v_cvt_pk_f32_fp8_e32 v[228:229], v140
	v_cvt_pk_f32_fp8_sdwa v[230:231], v140 src0_sel:WORD_1
	v_lshlrev_b32_e32 v208, 16, v152
	v_and_b32_e32 v209, 0xffff0000, v152
	v_lshlrev_b32_e32 v210, 16, v153
	v_and_b32_e32 v211, 0xffff0000, v153
	v_pk_fma_f32 v[208:209], v[224:225], v[240:241], v[208:209] op_sel_hi:[1,0,1]
	v_pk_fma_f32 v[210:211], v[226:227], v[240:241], v[210:211] op_sel_hi:[1,0,1]
	v_pk_fma_f32 v[208:209], v[228:229], v[242:243], v[208:209] op_sel_hi:[1,0,1]
	v_pk_fma_f32 v[210:211], v[230:231], v[242:243], v[210:211] op_sel_hi:[1,0,1]
	v_cvt_pk_f32_fp8_e32 v[232:233], v133
	v_cvt_pk_f32_fp8_sdwa v[234:235], v133 src0_sel:WORD_1
	v_cvt_pk_f32_fp8_e32 v[236:237], v141
	v_cvt_pk_f32_fp8_sdwa v[238:239], v141 src0_sel:WORD_1
	v_lshlrev_b32_e32 v212, 16, v154
	v_and_b32_e32 v213, 0xffff0000, v154
	v_lshlrev_b32_e32 v214, 16, v155
	v_and_b32_e32 v215, 0xffff0000, v155
	v_pk_fma_f32 v[212:213], v[232:233], v[240:241], v[212:213] op_sel_hi:[1,0,1]
	v_pk_fma_f32 v[214:215], v[234:235], v[240:241], v[214:215] op_sel_hi:[1,0,1]
	v_pk_fma_f32 v[212:213], v[236:237], v[242:243], v[212:213] op_sel_hi:[1,0,1]
	v_pk_fma_f32 v[214:215], v[238:239], v[242:243], v[214:215] op_sel_hi:[1,0,1]
	v_cvt_pk_f32_fp8_e32 v[224:225], v134
	v_cvt_pk_f32_fp8_sdwa v[226:227], v134 src0_sel:WORD_1
	v_cvt_pk_f32_fp8_e32 v[228:229], v142
	v_cvt_pk_f32_fp8_sdwa v[230:231], v142 src0_sel:WORD_1
	v_lshlrev_b32_e32 v216, 16, v156
	v_and_b32_e32 v217, 0xffff0000, v156
	v_lshlrev_b32_e32 v218, 16, v157
	v_and_b32_e32 v219, 0xffff0000, v157
	v_pk_fma_f32 v[216:217], v[224:225], v[240:241], v[216:217] op_sel_hi:[1,0,1]
	v_pk_fma_f32 v[218:219], v[226:227], v[240:241], v[218:219] op_sel_hi:[1,0,1]
	v_pk_fma_f32 v[216:217], v[228:229], v[242:243], v[216:217] op_sel_hi:[1,0,1]
	v_pk_fma_f32 v[218:219], v[230:231], v[242:243], v[218:219] op_sel_hi:[1,0,1]
	v_cvt_pk_f32_fp8_e32 v[232:233], v135
	v_cvt_pk_f32_fp8_sdwa v[234:235], v135 src0_sel:WORD_1
	v_cvt_pk_f32_fp8_e32 v[236:237], v143
	v_cvt_pk_f32_fp8_sdwa v[238:239], v143 src0_sel:WORD_1
	v_lshlrev_b32_e32 v220, 16, v158
	v_and_b32_e32 v221, 0xffff0000, v158
	v_lshlrev_b32_e32 v222, 16, v159
	v_and_b32_e32 v223, 0xffff0000, v159
	v_pk_fma_f32 v[220:221], v[232:233], v[240:241], v[220:221] op_sel_hi:[1,0,1]
	v_pk_fma_f32 v[222:223], v[234:235], v[240:241], v[222:223] op_sel_hi:[1,0,1]
	v_pk_fma_f32 v[220:221], v[236:237], v[242:243], v[220:221] op_sel_hi:[1,0,1]
	v_pk_fma_f32 v[222:223], v[238:239], v[242:243], v[222:223] op_sel_hi:[1,0,1]
	s_waitcnt vmcnt(55)
	s_add_u32 s56, s64, 0x5000000
	s_addc_u32 s57, s65, 0
	s_add_u32 s58, s56, 0x1000
	s_addc_u32 s59, s57, 0
	global_store_dwordx4 v4, v[192:195], s[56:57]
	global_store_dwordx4 v4, v[196:199], s[56:57] offset:1024
	global_store_dwordx4 v4, v[200:203], s[56:57] offset:2048
	global_store_dwordx4 v4, v[204:207], s[56:57] offset:3072
	global_store_dwordx4 v4, v[208:211], s[58:59]
	global_store_dwordx4 v4, v[212:215], s[58:59] offset:1024
	global_store_dwordx4 v4, v[216:219], s[58:59] offset:2048
	global_store_dwordx4 v4, v[220:223], s[58:59] offset:3072
	s_waitcnt vmcnt(32)
	v_mov_b32_e32 v240, s38
	v_mov_b32_e32 v242, s46
	v_cvt_pk_f32_fp8_e32 v[224:225], v64
	v_cvt_pk_f32_fp8_sdwa v[226:227], v64 src0_sel:WORD_1
	v_cvt_pk_f32_fp8_e32 v[228:229], v72
	v_cvt_pk_f32_fp8_sdwa v[230:231], v72 src0_sel:WORD_1
	v_lshlrev_b32_e32 v192, 16, v80
	v_and_b32_e32 v193, 0xffff0000, v80
	v_lshlrev_b32_e32 v194, 16, v81
	v_and_b32_e32 v195, 0xffff0000, v81
	v_pk_fma_f32 v[192:193], v[224:225], v[240:241], v[192:193] op_sel_hi:[1,0,1]
	v_pk_fma_f32 v[194:195], v[226:227], v[240:241], v[194:195] op_sel_hi:[1,0,1]
	v_pk_fma_f32 v[192:193], v[228:229], v[242:243], v[192:193] op_sel_hi:[1,0,1]
	v_pk_fma_f32 v[194:195], v[230:231], v[242:243], v[194:195] op_sel_hi:[1,0,1]
	v_cvt_pk_f32_fp8_e32 v[232:233], v65
	v_cvt_pk_f32_fp8_sdwa v[234:235], v65 src0_sel:WORD_1
	v_cvt_pk_f32_fp8_e32 v[236:237], v73
	v_cvt_pk_f32_fp8_sdwa v[238:239], v73 src0_sel:WORD_1
	v_lshlrev_b32_e32 v196, 16, v82
	v_and_b32_e32 v197, 0xffff0000, v82
	v_lshlrev_b32_e32 v198, 16, v83
	v_and_b32_e32 v199, 0xffff0000, v83
	v_pk_fma_f32 v[196:197], v[232:233], v[240:241], v[196:197] op_sel_hi:[1,0,1]
	v_pk_fma_f32 v[198:199], v[234:235], v[240:241], v[198:199] op_sel_hi:[1,0,1]
	v_pk_fma_f32 v[196:197], v[236:237], v[242:243], v[196:197] op_sel_hi:[1,0,1]
	v_pk_fma_f32 v[198:199], v[238:239], v[242:243], v[198:199] op_sel_hi:[1,0,1]
	v_cvt_pk_f32_fp8_e32 v[224:225], v66
	v_cvt_pk_f32_fp8_sdwa v[226:227], v66 src0_sel:WORD_1
	v_cvt_pk_f32_fp8_e32 v[228:229], v74
	v_cvt_pk_f32_fp8_sdwa v[230:231], v74 src0_sel:WORD_1
	v_lshlrev_b32_e32 v200, 16, v84
	v_and_b32_e32 v201, 0xffff0000, v84
	v_lshlrev_b32_e32 v202, 16, v85
	v_and_b32_e32 v203, 0xffff0000, v85
	v_pk_fma_f32 v[200:201], v[224:225], v[240:241], v[200:201] op_sel_hi:[1,0,1]
	v_pk_fma_f32 v[202:203], v[226:227], v[240:241], v[202:203] op_sel_hi:[1,0,1]
	v_pk_fma_f32 v[200:201], v[228:229], v[242:243], v[200:201] op_sel_hi:[1,0,1]
	v_pk_fma_f32 v[202:203], v[230:231], v[242:243], v[202:203] op_sel_hi:[1,0,1]
	v_cvt_pk_f32_fp8_e32 v[232:233], v67
	v_cvt_pk_f32_fp8_sdwa v[234:235], v67 src0_sel:WORD_1
	v_cvt_pk_f32_fp8_e32 v[236:237], v75
	v_cvt_pk_f32_fp8_sdwa v[238:239], v75 src0_sel:WORD_1
	v_lshlrev_b32_e32 v204, 16, v86
	v_and_b32_e32 v205, 0xffff0000, v86
	v_lshlrev_b32_e32 v206, 16, v87
	v_and_b32_e32 v207, 0xffff0000, v87
	v_pk_fma_f32 v[204:205], v[232:233], v[240:241], v[204:205] op_sel_hi:[1,0,1]
	v_pk_fma_f32 v[206:207], v[234:235], v[240:241], v[206:207] op_sel_hi:[1,0,1]
	v_pk_fma_f32 v[204:205], v[236:237], v[242:243], v[204:205] op_sel_hi:[1,0,1]
	v_pk_fma_f32 v[206:207], v[238:239], v[242:243], v[206:207] op_sel_hi:[1,0,1]
	v_cvt_pk_f32_fp8_e32 v[224:225], v68
	v_cvt_pk_f32_fp8_sdwa v[226:227], v68 src0_sel:WORD_1
	v_cvt_pk_f32_fp8_e32 v[228:229], v76
	v_cvt_pk_f32_fp8_sdwa v[230:231], v76 src0_sel:WORD_1
	v_lshlrev_b32_e32 v208, 16, v88
	v_and_b32_e32 v209, 0xffff0000, v88
	v_lshlrev_b32_e32 v210, 16, v89
	v_and_b32_e32 v211, 0xffff0000, v89
	v_pk_fma_f32 v[208:209], v[224:225], v[240:241], v[208:209] op_sel_hi:[1,0,1]
	v_pk_fma_f32 v[210:211], v[226:227], v[240:241], v[210:211] op_sel_hi:[1,0,1]
	v_pk_fma_f32 v[208:209], v[228:229], v[242:243], v[208:209] op_sel_hi:[1,0,1]
	v_pk_fma_f32 v[210:211], v[230:231], v[242:243], v[210:211] op_sel_hi:[1,0,1]
	v_cvt_pk_f32_fp8_e32 v[232:233], v69
	v_cvt_pk_f32_fp8_sdwa v[234:235], v69 src0_sel:WORD_1
	v_cvt_pk_f32_fp8_e32 v[236:237], v77
	v_cvt_pk_f32_fp8_sdwa v[238:239], v77 src0_sel:WORD_1
	v_lshlrev_b32_e32 v212, 16, v90
	v_and_b32_e32 v213, 0xffff0000, v90
	v_lshlrev_b32_e32 v214, 16, v91
	v_and_b32_e32 v215, 0xffff0000, v91
	v_pk_fma_f32 v[212:213], v[232:233], v[240:241], v[212:213] op_sel_hi:[1,0,1]
	v_pk_fma_f32 v[214:215], v[234:235], v[240:241], v[214:215] op_sel_hi:[1,0,1]
	v_pk_fma_f32 v[212:213], v[236:237], v[242:243], v[212:213] op_sel_hi:[1,0,1]
	v_pk_fma_f32 v[214:215], v[238:239], v[242:243], v[214:215] op_sel_hi:[1,0,1]
	v_cvt_pk_f32_fp8_e32 v[224:225], v70
	v_cvt_pk_f32_fp8_sdwa v[226:227], v70 src0_sel:WORD_1
	v_cvt_pk_f32_fp8_e32 v[228:229], v78
	v_cvt_pk_f32_fp8_sdwa v[230:231], v78 src0_sel:WORD_1
	v_lshlrev_b32_e32 v216, 16, v92
	v_and_b32_e32 v217, 0xffff0000, v92
	v_lshlrev_b32_e32 v218, 16, v93
	v_and_b32_e32 v219, 0xffff0000, v93
	v_pk_fma_f32 v[216:217], v[224:225], v[240:241], v[216:217] op_sel_hi:[1,0,1]
	v_pk_fma_f32 v[218:219], v[226:227], v[240:241], v[218:219] op_sel_hi:[1,0,1]
	v_pk_fma_f32 v[216:217], v[228:229], v[242:243], v[216:217] op_sel_hi:[1,0,1]
	v_pk_fma_f32 v[218:219], v[230:231], v[242:243], v[218:219] op_sel_hi:[1,0,1]
	v_cvt_pk_f32_fp8_e32 v[232:233], v71
	v_cvt_pk_f32_fp8_sdwa v[234:235], v71 src0_sel:WORD_1
	v_cvt_pk_f32_fp8_e32 v[236:237], v79
	v_cvt_pk_f32_fp8_sdwa v[238:239], v79 src0_sel:WORD_1
	v_lshlrev_b32_e32 v220, 16, v94
	v_and_b32_e32 v221, 0xffff0000, v94
	v_lshlrev_b32_e32 v222, 16, v95
	v_and_b32_e32 v223, 0xffff0000, v95
	v_pk_fma_f32 v[220:221], v[232:233], v[240:241], v[220:221] op_sel_hi:[1,0,1]
	v_pk_fma_f32 v[222:223], v[234:235], v[240:241], v[222:223] op_sel_hi:[1,0,1]
	v_pk_fma_f32 v[220:221], v[236:237], v[242:243], v[220:221] op_sel_hi:[1,0,1]
	v_pk_fma_f32 v[222:223], v[238:239], v[242:243], v[222:223] op_sel_hi:[1,0,1]
	s_waitcnt vmcnt(55)
	s_add_u32 s56, s64, 0x6000000
	s_addc_u32 s57, s65, 0
	s_add_u32 s58, s56, 0x1000
	s_addc_u32 s59, s57, 0
	global_store_dwordx4 v4, v[192:195], s[56:57]
	global_store_dwordx4 v4, v[196:199], s[56:57] offset:1024
	global_store_dwordx4 v4, v[200:203], s[56:57] offset:2048
	global_store_dwordx4 v4, v[204:207], s[56:57] offset:3072
	global_store_dwordx4 v4, v[208:211], s[58:59]
	global_store_dwordx4 v4, v[212:215], s[58:59] offset:1024
	global_store_dwordx4 v4, v[216:219], s[58:59] offset:2048
	global_store_dwordx4 v4, v[220:223], s[58:59] offset:3072
	s_waitcnt vmcnt(16)
	v_mov_b32_e32 v240, s39
	v_mov_b32_e32 v242, s47
	v_cvt_pk_f32_fp8_e32 v[224:225], v96
	v_cvt_pk_f32_fp8_sdwa v[226:227], v96 src0_sel:WORD_1
	v_cvt_pk_f32_fp8_e32 v[228:229], v104
	v_cvt_pk_f32_fp8_sdwa v[230:231], v104 src0_sel:WORD_1
	v_lshlrev_b32_e32 v192, 16, v112
	v_and_b32_e32 v193, 0xffff0000, v112
	v_lshlrev_b32_e32 v194, 16, v113
	v_and_b32_e32 v195, 0xffff0000, v113
	v_pk_fma_f32 v[192:193], v[224:225], v[240:241], v[192:193] op_sel_hi:[1,0,1]
	v_pk_fma_f32 v[194:195], v[226:227], v[240:241], v[194:195] op_sel_hi:[1,0,1]
	v_pk_fma_f32 v[192:193], v[228:229], v[242:243], v[192:193] op_sel_hi:[1,0,1]
	v_pk_fma_f32 v[194:195], v[230:231], v[242:243], v[194:195] op_sel_hi:[1,0,1]
	v_cvt_pk_f32_fp8_e32 v[232:233], v97
	v_cvt_pk_f32_fp8_sdwa v[234:235], v97 src0_sel:WORD_1
	v_cvt_pk_f32_fp8_e32 v[236:237], v105
	v_cvt_pk_f32_fp8_sdwa v[238:239], v105 src0_sel:WORD_1
	v_lshlrev_b32_e32 v196, 16, v114
	v_and_b32_e32 v197, 0xffff0000, v114
	v_lshlrev_b32_e32 v198, 16, v115
	v_and_b32_e32 v199, 0xffff0000, v115
	v_pk_fma_f32 v[196:197], v[232:233], v[240:241], v[196:197] op_sel_hi:[1,0,1]
	v_pk_fma_f32 v[198:199], v[234:235], v[240:241], v[198:199] op_sel_hi:[1,0,1]
	v_pk_fma_f32 v[196:197], v[236:237], v[242:243], v[196:197] op_sel_hi:[1,0,1]
	v_pk_fma_f32 v[198:199], v[238:239], v[242:243], v[198:199] op_sel_hi:[1,0,1]
	v_cvt_pk_f32_fp8_e32 v[224:225], v98
	v_cvt_pk_f32_fp8_sdwa v[226:227], v98 src0_sel:WORD_1
	v_cvt_pk_f32_fp8_e32 v[228:229], v106
	v_cvt_pk_f32_fp8_sdwa v[230:231], v106 src0_sel:WORD_1
	v_lshlrev_b32_e32 v200, 16, v116
	v_and_b32_e32 v201, 0xffff0000, v116
	v_lshlrev_b32_e32 v202, 16, v117
	v_and_b32_e32 v203, 0xffff0000, v117
	v_pk_fma_f32 v[200:201], v[224:225], v[240:241], v[200:201] op_sel_hi:[1,0,1]
	v_pk_fma_f32 v[202:203], v[226:227], v[240:241], v[202:203] op_sel_hi:[1,0,1]
	v_pk_fma_f32 v[200:201], v[228:229], v[242:243], v[200:201] op_sel_hi:[1,0,1]
	v_pk_fma_f32 v[202:203], v[230:231], v[242:243], v[202:203] op_sel_hi:[1,0,1]
	v_cvt_pk_f32_fp8_e32 v[232:233], v99
	v_cvt_pk_f32_fp8_sdwa v[234:235], v99 src0_sel:WORD_1
	v_cvt_pk_f32_fp8_e32 v[236:237], v107
	v_cvt_pk_f32_fp8_sdwa v[238:239], v107 src0_sel:WORD_1
	v_lshlrev_b32_e32 v204, 16, v118
	v_and_b32_e32 v205, 0xffff0000, v118
	v_lshlrev_b32_e32 v206, 16, v119
	v_and_b32_e32 v207, 0xffff0000, v119
	v_pk_fma_f32 v[204:205], v[232:233], v[240:241], v[204:205] op_sel_hi:[1,0,1]
	v_pk_fma_f32 v[206:207], v[234:235], v[240:241], v[206:207] op_sel_hi:[1,0,1]
	v_pk_fma_f32 v[204:205], v[236:237], v[242:243], v[204:205] op_sel_hi:[1,0,1]
	v_pk_fma_f32 v[206:207], v[238:239], v[242:243], v[206:207] op_sel_hi:[1,0,1]
	v_cvt_pk_f32_fp8_e32 v[224:225], v100
	v_cvt_pk_f32_fp8_sdwa v[226:227], v100 src0_sel:WORD_1
	v_cvt_pk_f32_fp8_e32 v[228:229], v108
	v_cvt_pk_f32_fp8_sdwa v[230:231], v108 src0_sel:WORD_1
	v_lshlrev_b32_e32 v208, 16, v120
	v_and_b32_e32 v209, 0xffff0000, v120
	v_lshlrev_b32_e32 v210, 16, v121
	v_and_b32_e32 v211, 0xffff0000, v121
	v_pk_fma_f32 v[208:209], v[224:225], v[240:241], v[208:209] op_sel_hi:[1,0,1]
	v_pk_fma_f32 v[210:211], v[226:227], v[240:241], v[210:211] op_sel_hi:[1,0,1]
	v_pk_fma_f32 v[208:209], v[228:229], v[242:243], v[208:209] op_sel_hi:[1,0,1]
	v_pk_fma_f32 v[210:211], v[230:231], v[242:243], v[210:211] op_sel_hi:[1,0,1]
	v_cvt_pk_f32_fp8_e32 v[232:233], v101
	v_cvt_pk_f32_fp8_sdwa v[234:235], v101 src0_sel:WORD_1
	v_cvt_pk_f32_fp8_e32 v[236:237], v109
	v_cvt_pk_f32_fp8_sdwa v[238:239], v109 src0_sel:WORD_1
	v_lshlrev_b32_e32 v212, 16, v122
	v_and_b32_e32 v213, 0xffff0000, v122
	v_lshlrev_b32_e32 v214, 16, v123
	v_and_b32_e32 v215, 0xffff0000, v123
	v_pk_fma_f32 v[212:213], v[232:233], v[240:241], v[212:213] op_sel_hi:[1,0,1]
	v_pk_fma_f32 v[214:215], v[234:235], v[240:241], v[214:215] op_sel_hi:[1,0,1]
	v_pk_fma_f32 v[212:213], v[236:237], v[242:243], v[212:213] op_sel_hi:[1,0,1]
	v_pk_fma_f32 v[214:215], v[238:239], v[242:243], v[214:215] op_sel_hi:[1,0,1]
	v_cvt_pk_f32_fp8_e32 v[224:225], v102
	v_cvt_pk_f32_fp8_sdwa v[226:227], v102 src0_sel:WORD_1
	v_cvt_pk_f32_fp8_e32 v[228:229], v110
	v_cvt_pk_f32_fp8_sdwa v[230:231], v110 src0_sel:WORD_1
	v_lshlrev_b32_e32 v216, 16, v124
	v_and_b32_e32 v217, 0xffff0000, v124
	v_lshlrev_b32_e32 v218, 16, v125
	v_and_b32_e32 v219, 0xffff0000, v125
	v_pk_fma_f32 v[216:217], v[224:225], v[240:241], v[216:217] op_sel_hi:[1,0,1]
	v_pk_fma_f32 v[218:219], v[226:227], v[240:241], v[218:219] op_sel_hi:[1,0,1]
	v_pk_fma_f32 v[216:217], v[228:229], v[242:243], v[216:217] op_sel_hi:[1,0,1]
	v_pk_fma_f32 v[218:219], v[230:231], v[242:243], v[218:219] op_sel_hi:[1,0,1]
	v_cvt_pk_f32_fp8_e32 v[232:233], v103
	v_cvt_pk_f32_fp8_sdwa v[234:235], v103 src0_sel:WORD_1
	v_cvt_pk_f32_fp8_e32 v[236:237], v111
	v_cvt_pk_f32_fp8_sdwa v[238:239], v111 src0_sel:WORD_1
	v_lshlrev_b32_e32 v220, 16, v126
	v_and_b32_e32 v221, 0xffff0000, v126
	v_lshlrev_b32_e32 v222, 16, v127
	v_and_b32_e32 v223, 0xffff0000, v127
	v_pk_fma_f32 v[220:221], v[232:233], v[240:241], v[220:221] op_sel_hi:[1,0,1]
	v_pk_fma_f32 v[222:223], v[234:235], v[240:241], v[222:223] op_sel_hi:[1,0,1]
	v_pk_fma_f32 v[220:221], v[236:237], v[242:243], v[220:221] op_sel_hi:[1,0,1]
	v_pk_fma_f32 v[222:223], v[238:239], v[242:243], v[222:223] op_sel_hi:[1,0,1]
	s_waitcnt vmcnt(55)
	s_add_u32 s56, s64, 0x7000000
	s_addc_u32 s57, s65, 0
	s_add_u32 s58, s56, 0x1000
	s_addc_u32 s59, s57, 0
	global_store_dwordx4 v4, v[192:195], s[56:57]
	global_store_dwordx4 v4, v[196:199], s[56:57] offset:1024
	global_store_dwordx4 v4, v[200:203], s[56:57] offset:2048
	global_store_dwordx4 v4, v[204:207], s[56:57] offset:3072
	global_store_dwordx4 v4, v[208:211], s[58:59]
	global_store_dwordx4 v4, v[212:215], s[58:59] offset:1024
	global_store_dwordx4 v4, v[216:219], s[58:59] offset:2048
	global_store_dwordx4 v4, v[220:223], s[58:59] offset:3072
